# nt on the remaining read-once input streams of P0 (p, keys, small weight transposes) and the attention Q-row loads
# speedup vs baseline: 1.0046x; 1.0046x over previous
; __device__ __forceinline__ unsigned pk2(float lo, float hi) { return f2bf(lo) | (f2bf(hi) << 16); }
; __device__ __forceinline__ void transpose_item(const float* src, int ld_src, int nvalid, bf16_t* dst, int ld_dst, int nblk, int item, int lane) {
;     const int kb = item / nblk, nb = item % nblk, nq = lane & 15, kg = lane >> 4, k = 32 * kb + 8 * kg, n = 64 * nb + 4 * nq;
;     f32x4 v[8];
;     const bool ok = n < nvalid;
; #pragma unroll
;     for (int i = 0; i < 8; ++i) v[i] = ok ? *(const f32x4*)(src + (size_t)(k + i) * ld_src + n) : (f32x4){0.f, 0.f, 0.f, 0.f};
; #pragma unroll
;     for (int jn = 0; jn < 4; ++jn) { u32x4 o; o.x = pk2(v[0][jn], v[1][jn]); o.y = pk2(v[2][jn], v[3][jn]); o.z = pk2(v[4][jn], v[5][jn]); o.w = pk2(v[6][jn], v[7][jn]);
;         *(u32x4*)(dst + (size_t)(n + jn) * ld_dst + k) = o; }
; }
; __device__ __forceinline__ void phase_prologue(const Frame& F, const Args& a) {
;     ...
;           else { const int j = (it - J1) >> 7, kv = j >> 1, half = j & 1;
;               transpose_item(a.in[8 + kv] + (size_t)half * 2048 * 128, 128, 128, (bf16_t*)(ws + WS_W_CMP) + (size_t)(kv * 256 + half * 128) * 2048, 2048, 2, (it - J1) & 127, F.lane); } } }
.LBB0_46:
	s_cmpk_gt_i32 s42, 0x1ff
	s_mov_b64 s[20:21], -1
	s_cbranch_scc0 .LBB0_52
	s_cmpk_gt_u32 s42, 0x3ff
	s_cbranch_scc0 .LBB0_49
	s_add_i32 s16, s42, 0xfffffc00
	s_lshr_b32 s20, s16, 5
	s_and_b32 s20, s20, 0x7fffff8
	s_load_dwordx2 s[20:21], s[86:87], s20 offset:0x40
	s_bfe_u32 s43, s42, 0x10007
	s_lshl_b32 s44, s43, 20
	v_and_or_b32 v38, s30, 64, v1
	v_lshlrev_b32_e32 v34, 2, v38
	s_waitcnt lgkmcnt(0)
	s_add_u32 s20, s20, s44
	s_addc_u32 s21, s21, 0
	s_and_b32 s16, s16, 0xffffff00
	s_lshl_b32 s43, s43, 7
	s_or_b32 s16, s43, s16
	s_lshl_b64 s[44:45], s[16:17], 12
	s_add_u32 s44, s26, s44
	s_addc_u32 s45, s27, s45
	s_and_b32 s16, s33, 0x7e0
	v_or_b32_e32 v36, s16, v42
	v_lshl_add_u64 v[2:3], s[20:21], 0, v[34:35]
	v_lshlrev_b32_e32 v34, 9, v36
	v_lshl_add_u64 v[30:31], v[2:3], 0, v[34:35]
	global_load_dwordx4 v[2:5], v[30:31], off nt
	global_load_dwordx4 v[6:9], v[30:31], off offset:512 nt
	global_load_dwordx4 v[10:13], v[30:31], off offset:1024 nt
	global_load_dwordx4 v[14:17], v[30:31], off offset:1536 nt
	global_load_dwordx4 v[18:21], v[30:31], off offset:2048 nt
	global_load_dwordx4 v[22:25], v[30:31], off offset:2560 nt
	global_load_dwordx4 v[26:29], v[30:31], off offset:3072 nt
	s_nop 0
	global_load_dwordx4 v[30:33], v[30:31], off offset:3584 nt
	v_lshlrev_b32_e32 v34, 1, v36
	v_lshl_add_u64 v[36:37], s[44:45], 0, v[34:35]
	v_lshlrev_b32_e32 v34, 12, v38
	v_lshl_add_u64 v[40:41], v[36:37], 0, v[34:35]
	v_add_co_u32_e32 v52, vcc, s40, v40
	s_mov_b64 s[20:21], 0
	s_nop 0
	v_addc_co_u32_e32 v53, vcc, 0, v41, vcc
	s_waitcnt vmcnt(7)
	v_bfe_u32 v34, v2, 16, 1
	s_waitcnt vmcnt(6)
	v_bfe_u32 v36, v6, 16, 1
	v_add3_u32 v2, v2, v34, s37
	v_add3_u32 v6, v6, v36, s37
	s_waitcnt vmcnt(3)
	v_bfe_u32 v60, v20, 16, 1
	v_lshrrev_b32_e32 v2, 16, v2
	v_bfe_u32 v46, v3, 16, 1
	v_add3_u32 v20, v20, v60, s37
	v_and_or_b32 v36, v6, s38, v2
	s_waitcnt vmcnt(2)
	v_bfe_u32 v2, v24, 16, 1
	v_bfe_u32 v47, v7, 16, 1
	v_bfe_u32 v50, v19, 16, 1
	v_add3_u32 v3, v3, v46, s37
	v_lshrrev_b32_e32 v20, 16, v20
	v_add3_u32 v2, v24, v2, s37
	s_waitcnt vmcnt(1)
	v_bfe_u32 v44, v26, 16, 1
	v_add3_u32 v7, v7, v47, s37
	v_add3_u32 v19, v19, v50, s37
	v_lshrrev_b32_e32 v3, 16, v3
	v_and_or_b32 v50, v2, s38, v20
	v_bfe_u32 v2, v28, 16, 1
	v_add3_u32 v26, v26, v44, s37
	v_and_or_b32 v44, v7, s38, v3
	v_add3_u32 v2, v28, v2, s37
	s_waitcnt vmcnt(0)
	v_bfe_u32 v3, v32, 16, 1
	v_bfe_u32 v51, v23, 16, 1
	v_lshrrev_b32_e32 v2, 16, v2
	v_add3_u32 v3, v32, v3, s37
	v_add3_u32 v23, v23, v51, s37
	v_and_or_b32 v51, v3, s38, v2
	v_bfe_u32 v2, v5, 16, 1
	v_bfe_u32 v56, v4, 16, 1
	v_add3_u32 v2, v5, v2, s37
	v_bfe_u32 v3, v9, 16, 1
	v_bfe_u32 v57, v8, 16, 1
	v_add3_u32 v4, v4, v56, s37
	v_lshrrev_b32_e32 v2, 16, v2
	v_add3_u32 v3, v9, v3, s37
	v_bfe_u32 v48, v11, 16, 1
	v_add3_u32 v8, v8, v57, s37
	v_lshrrev_b32_e32 v4, 16, v4
	v_and_or_b32 v2, v3, s38, v2
	v_bfe_u32 v3, v13, 16, 1
	v_add3_u32 v11, v11, v48, s37
	v_and_or_b32 v48, v8, s38, v4
	v_add3_u32 v3, v13, v3, s37
	v_bfe_u32 v4, v17, 16, 1
	v_lshrrev_b32_e32 v3, 16, v3
	v_add3_u32 v4, v17, v4, s37
	v_and_or_b32 v3, v4, s38, v3
	v_bfe_u32 v4, v21, 16, 1
	v_add3_u32 v4, v21, v4, s37
	v_bfe_u32 v5, v25, 16, 1
	v_lshrrev_b32_e32 v4, 16, v4
	v_add3_u32 v5, v25, v5, s37
	v_and_or_b32 v4, v5, s38, v4
	v_bfe_u32 v5, v29, 16, 1
	v_bfe_u32 v37, v10, 16, 1
	v_bfe_u32 v39, v18, 16, 1
	v_bfe_u32 v58, v12, 16, 1
	v_add3_u32 v5, v29, v5, s37
	v_bfe_u32 v6, v33, 16, 1
	v_bfe_u32 v38, v14, 16, 1
	v_bfe_u32 v43, v22, 16, 1
	v_bfe_u32 v45, v30, 16, 1
	v_bfe_u32 v54, v27, 16, 1
	v_bfe_u32 v59, v16, 16, 1
	v_add3_u32 v10, v10, v37, s37
	v_add3_u32 v18, v18, v39, s37
	v_add3_u32 v12, v12, v58, s37
	v_lshrrev_b32_e32 v5, 16, v5
	v_add3_u32 v6, v33, v6, s37
	v_bfe_u32 v49, v15, 16, 1
	v_bfe_u32 v55, v31, 16, 1
	v_add3_u32 v14, v14, v38, s37
	v_add3_u32 v22, v22, v43, s37
	v_add3_u32 v30, v30, v45, s37
	v_add3_u32 v27, v27, v54, s37
	v_add3_u32 v16, v16, v59, s37
	v_lshrrev_b32_e32 v10, 16, v10
	v_lshrrev_b32_e32 v18, 16, v18
	v_lshrrev_b32_e32 v26, 16, v26
	v_lshrrev_b32_e32 v12, 16, v12
	v_and_or_b32 v5, v6, s38, v5
	v_add_co_u32_e32 v6, vcc, 0x3000, v40
	v_add3_u32 v15, v15, v49, s37
	v_add3_u32 v31, v31, v55, s37
	v_lshrrev_b32_e32 v11, 16, v11
	v_lshrrev_b32_e32 v19, 16, v19
	v_lshrrev_b32_e32 v27, 16, v27
	v_and_or_b32 v37, v14, s38, v10
	v_and_or_b32 v38, v22, s38, v18
	v_and_or_b32 v39, v30, s38, v26
	v_and_or_b32 v49, v16, s38, v12
	v_addc_co_u32_e32 v7, vcc, 0, v41, vcc
	v_and_or_b32 v45, v15, s38, v11
	v_and_or_b32 v46, v23, s38, v19
	v_and_or_b32 v47, v31, s38, v27
	global_store_dwordx4 v[40:41], v[36:39], off
	global_store_dwordx4 v[52:53], v[44:47], off offset:-4096
	global_store_dwordx4 v[52:53], v[48:51], off
	global_store_dwordx4 v[6:7], v[2:5], off
; __device__ __forceinline__ unsigned pk2(float lo, float hi) { return f2bf(lo) | (f2bf(hi) << 16); }
; __device__ __forceinline__ void transpose_item(const float* src, int ld_src, int nvalid, bf16_t* dst, int ld_dst, int nblk, int item, int lane) {
;     const int kb = item / nblk, nb = item % nblk, nq = lane & 15, kg = lane >> 4, k = 32 * kb + 8 * kg, n = 64 * nb + 4 * nq;
;     f32x4 v[8];
;     const bool ok = n < nvalid;
; #pragma unroll
;     for (int i = 0; i < 8; ++i) v[i] = ok ? *(const f32x4*)(src + (size_t)(k + i) * ld_src + n) : (f32x4){0.f, 0.f, 0.f, 0.f};
; #pragma unroll
;     for (int jn = 0; jn < 4; ++jn) { u32x4 o; o.x = pk2(v[0][jn], v[1][jn]); o.y = pk2(v[2][jn], v[3][jn]); o.z = pk2(v[4][jn], v[5][jn]); o.w = pk2(v[6][jn], v[7][jn]);
;         *(u32x4*)(dst + (size_t)(n + jn) * ld_dst + k) = o; }
; }
; __device__ __forceinline__ void phase_prologue(const Frame& F, const Args& a) {
;     ...
;           else if (it < J1) { const int gi = (it - J0) >> 7; transpose_item(a.in[4] + (size_t)gi * 512 * 512, 512, 512, (bf16_t*)(ws + WS_W_POOL) + (size_t)gi * 512 * 512, 512, 8, (it - J0) & 127, F.lane); }
.LBB0_49:
	s_andn2_b64 vcc, exec, s[20:21]
	s_cbranch_vccnz .LBB0_51
	s_add_i32 s16, s42, 0xfffffe00
	s_lshr_b32 s16, s16, 7
	s_lshl_b64 s[20:21], s[16:17], 20
	s_add_u32 s20, s24, s20
	s_addc_u32 s21, s25, s21
	s_lshl_b64 s[44:45], s[16:17], 19
	s_add_u32 s44, s28, s44
	s_addc_u32 s45, s29, s45
	s_and_b32 s16, s35, 0x1e0
	v_or_b32_e32 v36, s16, v42
	s_and_b32 s16, s30, 0x1c0
	v_or_b32_e32 v38, s16, v1
	v_lshlrev_b32_e32 v34, 2, v38
	v_lshl_add_u64 v[2:3], s[20:21], 0, v[34:35]
	v_lshlrev_b32_e32 v34, 11, v36
	v_lshl_add_u64 v[26:27], v[2:3], 0, v[34:35]
	v_add_co_u32_e32 v14, vcc, s39, v26
	global_load_dwordx4 v[2:5], v[26:27], off nt
	global_load_dwordx4 v[6:9], v[26:27], off offset:2048 nt
	v_addc_co_u32_e32 v15, vcc, 0, v27, vcc
	v_add_co_u32_e32 v22, vcc, s40, v26
	v_lshlrev_b32_e32 v34, 1, v36
	s_nop 0
	v_addc_co_u32_e32 v23, vcc, 0, v27, vcc
	global_load_dwordx4 v[10:13], v[22:23], off offset:-4096 nt
	s_nop 0
	global_load_dwordx4 v[14:17], v[14:15], off offset:2048 nt
	s_nop 0
	global_load_dwordx4 v[18:21], v[22:23], off nt
	s_nop 0
	global_load_dwordx4 v[22:25], v[22:23], off offset:2048 nt
	v_add_co_u32_e32 v30, vcc, s41, v26
	v_lshl_add_u64 v[36:37], s[44:45], 0, v[34:35]
	s_nop 0
	v_addc_co_u32_e32 v31, vcc, 0, v27, vcc
	global_load_dwordx4 v[26:29], v[30:31], off nt
	s_nop 0
	global_load_dwordx4 v[30:33], v[30:31], off offset:2048 nt
	v_lshlrev_b32_e32 v34, 10, v38
	v_lshl_add_u64 v[40:41], v[36:37], 0, v[34:35]
	s_waitcnt vmcnt(7)
	v_bfe_u32 v34, v2, 16, 1
	v_bfe_u32 v37, v3, 16, 1
	s_waitcnt vmcnt(6)
	v_bfe_u32 v36, v6, 16, 1
	v_bfe_u32 v38, v7, 16, 1
	v_add3_u32 v2, v2, v34, s37
	v_add3_u32 v3, v3, v37, s37
	s_waitcnt vmcnt(5)
	v_bfe_u32 v34, v10, 16, 1
	v_bfe_u32 v37, v11, 16, 1
	v_bfe_u32 v43, v8, 16, 1
	v_add3_u32 v6, v6, v36, s37
	s_waitcnt vmcnt(4)
	v_bfe_u32 v36, v14, 16, 1
	s_waitcnt vmcnt(3)
	v_bfe_u32 v44, v18, 16, 1
	v_add3_u32 v7, v7, v38, s37
	v_bfe_u32 v38, v15, 16, 1
	v_lshrrev_b32_e32 v2, 16, v2
	v_add3_u32 v10, v10, v34, s37
	v_lshrrev_b32_e32 v3, 16, v3
	v_add3_u32 v11, v11, v37, s37
	s_waitcnt vmcnt(2)
	v_bfe_u32 v45, v22, 16, 1
	v_add3_u32 v8, v8, v43, s37
	v_bfe_u32 v43, v12, 16, 1
	v_add3_u32 v14, v14, v36, s37
	v_add3_u32 v18, v18, v44, s37
	v_add3_u32 v15, v15, v38, s37
	v_and_or_b32 v36, v6, s38, v2
	v_lshrrev_b32_e32 v2, 16, v10
	v_and_or_b32 v44, v7, s38, v3
	v_lshrrev_b32_e32 v3, 16, v11
	v_add3_u32 v22, v22, v45, s37
	v_and_or_b32 v37, v14, s38, v2
	v_and_or_b32 v45, v15, s38, v3
	v_add3_u32 v2, v12, v43, s37
	v_bfe_u32 v3, v16, 16, 1
	v_bfe_u32 v49, v23, 16, 1
	v_lshrrev_b32_e32 v2, 16, v2
	v_add3_u32 v3, v16, v3, s37
	v_add3_u32 v23, v23, v49, s37
	v_and_or_b32 v49, v3, s38, v2
	v_bfe_u32 v2, v20, 16, 1
	v_add3_u32 v2, v20, v2, s37
	v_bfe_u32 v3, v24, 16, 1
	s_waitcnt vmcnt(1)
	v_bfe_u32 v50, v27, 16, 1
	v_lshrrev_b32_e32 v2, 16, v2
	v_add3_u32 v3, v24, v3, s37
	v_add3_u32 v27, v27, v50, s37
	v_and_or_b32 v50, v3, s38, v2
	v_bfe_u32 v2, v28, 16, 1
	v_add3_u32 v2, v28, v2, s37
	s_waitcnt vmcnt(0)
	v_bfe_u32 v3, v32, 16, 1
	v_bfe_u32 v51, v31, 16, 1
	v_lshrrev_b32_e32 v2, 16, v2
	v_add3_u32 v3, v32, v3, s37
	v_add3_u32 v31, v31, v51, s37
	v_and_or_b32 v51, v3, s38, v2
	v_bfe_u32 v2, v5, 16, 1
	v_bfe_u32 v39, v4, 16, 1
	v_add3_u32 v2, v5, v2, s37
	v_bfe_u32 v3, v9, 16, 1
	v_add3_u32 v4, v4, v39, s37
	v_lshrrev_b32_e32 v2, 16, v2
	v_add3_u32 v3, v9, v3, s37
	v_bfe_u32 v48, v19, 16, 1
	v_lshrrev_b32_e32 v4, 16, v4
	v_and_or_b32 v2, v3, s38, v2
	v_bfe_u32 v3, v13, 16, 1
	v_add3_u32 v19, v19, v48, s37
	v_and_or_b32 v48, v8, s38, v4
	v_add3_u32 v3, v13, v3, s37
	v_bfe_u32 v4, v17, 16, 1
	v_lshrrev_b32_e32 v3, 16, v3
	v_add3_u32 v4, v17, v4, s37
	v_and_or_b32 v3, v4, s38, v3
	v_bfe_u32 v4, v21, 16, 1
	v_add3_u32 v4, v21, v4, s37
	v_bfe_u32 v5, v25, 16, 1
	v_lshrrev_b32_e32 v4, 16, v4
	v_add3_u32 v5, v25, v5, s37
	v_bfe_u32 v46, v26, 16, 1
	v_lshrrev_b32_e32 v6, 16, v18
	v_and_or_b32 v4, v5, s38, v4
	v_bfe_u32 v5, v29, 16, 1
	v_bfe_u32 v47, v30, 16, 1
	v_add3_u32 v26, v26, v46, s37
	v_and_or_b32 v38, v22, s38, v6
	v_add3_u32 v5, v29, v5, s37
	v_bfe_u32 v6, v33, 16, 1
	v_add3_u32 v30, v30, v47, s37
	v_lshrrev_b32_e32 v10, 16, v26
	v_lshrrev_b32_e32 v5, 16, v5
	v_add3_u32 v6, v33, v6, s37
	v_lshrrev_b32_e32 v7, 16, v19
	v_lshrrev_b32_e32 v11, 16, v27
	v_and_or_b32 v39, v30, s38, v10
	v_and_or_b32 v5, v6, s38, v5
	v_and_or_b32 v46, v23, s38, v7
	v_and_or_b32 v47, v31, s38, v11
	global_store_dwordx4 v[40:41], v[36:39], off
	global_store_dwordx4 v[40:41], v[44:47], off offset:1024
	global_store_dwordx4 v[40:41], v[48:51], off offset:2048
	global_store_dwordx4 v[40:41], v[2:5], off offset:3072

; __device__ __forceinline__ unsigned pk2(float lo, float hi) { return f2bf(lo) | (f2bf(hi) << 16); }
; __device__ __forceinline__ void transpose_item(const float* src, int ld_src, int nvalid, bf16_t* dst, int ld_dst, int nblk, int item, int lane) {
;     const int kb = item / nblk, nb = item % nblk, nq = lane & 15, kg = lane >> 4, k = 32 * kb + 8 * kg, n = 64 * nb + 4 * nq;
;     f32x4 v[8];
;     const bool ok = n < nvalid;
; #pragma unroll
;     for (int i = 0; i < 8; ++i) v[i] = ok ? *(const f32x4*)(src + (size_t)(k + i) * ld_src + n) : (f32x4){0.f, 0.f, 0.f, 0.f};
; #pragma unroll
;     for (int jn = 0; jn < 4; ++jn) { u32x4 o; o.x = pk2(v[0][jn], v[1][jn]); o.y = pk2(v[2][jn], v[3][jn]); o.z = pk2(v[4][jn], v[5][jn]); o.w = pk2(v[6][jn], v[7][jn]);
;         *(u32x4*)(dst + (size_t)(n + jn) * ld_dst + k) = o; }
; }
; __device__ __forceinline__ void phase_prologue(const Frame& F, const Args& a) {
;     ...
;           if (it < J0) transpose_item(a.in[21], D, D, (bf16_t*)(ws + WS_W_PP), 256, 64, it, F.lane);
.LBB0_52:
	s_andn2_b64 vcc, exec, s[20:21]
	s_cbranch_vccnz .LBB0_45
	s_ashr_i32 s16, s42, 31
	s_lshr_b32 s16, s16, 26
	s_add_i32 s16, s42, s16
	s_ashr_i32 s16, s16, 6
	v_lshl_or_b32 v38, s16, 5, v42
	v_add_u32_e32 v2, s30, v1
	s_lshl_b32 s16, s16, 12
	v_subrev_u32_e32 v36, s16, v2
	v_ashrrev_i32_e32 v37, 31, v36
	v_cmp_gt_i32_e32 vcc, s39, v36
	v_lshl_add_u64 v[40:41], v[36:37], 2, s[22:23]
	v_mov_b32_e32 v2, 0
	v_ashrrev_i32_e32 v39, 31, v38
	v_mov_b32_e32 v6, 0
	v_mov_b32_e32 v7, 0
	v_mov_b32_e32 v8, 0
	v_mov_b32_e32 v9, 0
	s_and_saveexec_b64 s[20:21], vcc
	s_cbranch_execz .LBB0_55
	v_lshlrev_b64 v[4:5], 14, v[38:39]
	v_lshl_add_u64 v[4:5], v[40:41], 0, v[4:5]
	global_load_dwordx4 v[6:9], v[4:5], off nt
.LBB0_55:
	s_or_b64 exec, exec, s[20:21]
	v_mov_b32_e32 v3, 0
	v_mov_b32_e32 v4, 0
	v_mov_b32_e32 v5, 0
	s_and_saveexec_b64 s[20:21], vcc
	s_cbranch_execz .LBB0_57
	v_or_b32_e32 v2, 1, v38
	v_ashrrev_i32_e32 v3, 31, v2
	v_lshlrev_b64 v[2:3], 14, v[2:3]
	v_lshl_add_u64 v[2:3], v[40:41], 0, v[2:3]
	global_load_dwordx4 v[2:5], v[2:3], off nt
.LBB0_57:
	s_or_b64 exec, exec, s[20:21]
	v_mov_b32_e32 v10, 0
	v_mov_b32_e32 v14, 0
	v_mov_b32_e32 v15, 0
	v_mov_b32_e32 v16, 0
	v_mov_b32_e32 v17, 0
	s_and_saveexec_b64 s[20:21], vcc
	s_cbranch_execz .LBB0_59
	v_or_b32_e32 v12, 2, v38
	v_ashrrev_i32_e32 v13, 31, v12
	v_lshlrev_b64 v[12:13], 14, v[12:13]
	v_lshl_add_u64 v[12:13], v[40:41], 0, v[12:13]
	global_load_dwordx4 v[14:17], v[12:13], off nt
.LBB0_59:
	s_or_b64 exec, exec, s[20:21]
	v_mov_b32_e32 v11, 0
	v_mov_b32_e32 v12, 0
	v_mov_b32_e32 v13, 0
	s_and_saveexec_b64 s[20:21], vcc
	s_cbranch_execz .LBB0_61
	v_or_b32_e32 v10, 3, v38
	v_ashrrev_i32_e32 v11, 31, v10
	v_lshlrev_b64 v[10:11], 14, v[10:11]
	v_lshl_add_u64 v[10:11], v[40:41], 0, v[10:11]
	global_load_dwordx4 v[10:13], v[10:11], off nt
.LBB0_61:
	s_or_b64 exec, exec, s[20:21]
	v_mov_b32_e32 v18, 0
	v_mov_b32_e32 v22, 0
	v_mov_b32_e32 v23, 0
	v_mov_b32_e32 v24, 0
	v_mov_b32_e32 v25, 0
	s_and_saveexec_b64 s[20:21], vcc
	s_cbranch_execz .LBB0_63
	v_or_b32_e32 v20, 4, v38
	v_ashrrev_i32_e32 v21, 31, v20
	v_lshlrev_b64 v[20:21], 14, v[20:21]
	v_lshl_add_u64 v[20:21], v[40:41], 0, v[20:21]
	global_load_dwordx4 v[22:25], v[20:21], off nt
.LBB0_63:
	s_or_b64 exec, exec, s[20:21]
	v_mov_b32_e32 v19, 0
	v_mov_b32_e32 v20, 0
	v_mov_b32_e32 v21, 0
	s_and_saveexec_b64 s[20:21], vcc
	s_cbranch_execz .LBB0_65
	v_or_b32_e32 v18, 5, v38
	v_ashrrev_i32_e32 v19, 31, v18
	v_lshlrev_b64 v[18:19], 14, v[18:19]
	v_lshl_add_u64 v[18:19], v[40:41], 0, v[18:19]
	global_load_dwordx4 v[18:21], v[18:19], off nt
.LBB0_65:
	s_or_b64 exec, exec, s[20:21]
	v_mov_b32_e32 v26, 0
	v_mov_b32_e32 v30, 0
	v_mov_b32_e32 v31, 0
	v_mov_b32_e32 v32, 0
	v_mov_b32_e32 v33, 0
	s_and_saveexec_b64 s[20:21], vcc
	s_cbranch_execz .LBB0_67
	v_or_b32_e32 v28, 6, v38
	v_ashrrev_i32_e32 v29, 31, v28
	v_lshlrev_b64 v[28:29], 14, v[28:29]
	v_lshl_add_u64 v[28:29], v[40:41], 0, v[28:29]
	global_load_dwordx4 v[30:33], v[28:29], off nt
.LBB0_67:
	s_or_b64 exec, exec, s[20:21]
	v_mov_b32_e32 v27, 0
	v_mov_b32_e32 v28, 0
	v_mov_b32_e32 v29, 0
	s_and_saveexec_b64 s[20:21], vcc
	s_cbranch_execz .LBB0_44
	v_or_b32_e32 v26, 7, v38
	v_ashrrev_i32_e32 v27, 31, v26
	v_lshlrev_b64 v[26:27], 14, v[26:27]
	v_lshl_add_u64 v[26:27], v[40:41], 0, v[26:27]
	global_load_dwordx4 v[26:29], v[26:27], off nt
	s_branch .LBB0_44

; __device__ __forceinline__ unsigned pk2(float lo, float hi) { return f2bf(lo) | (f2bf(hi) << 16); }
; __device__ __forceinline__ void cvt_stream(const float* src, bf16_t* dst, size_t n8, size_t gtid, size_t gthreads) {
;     for (size_t i = gtid; i < n8; i += gthreads) { const f32x4 a = ((const f32x4*)src)[2 * i], b = ((const f32x4*)src)[2 * i + 1];
;         ((u32x4*)dst)[i] = (u32x4){pk2(a.x, a.y), pk2(a.z, a.w), pk2(b.x, b.y), pk2(b.z, b.w)}; }
; }
; __device__ __forceinline__ void phase_prologue(const Frame& F, const Args& a) {
;     ...
;     cvt_stream(a.in[1], (bf16_t*)(ws + WS_PBF), (size_t)T * 256 / 8, gtid, gth);
.LBB0_71:
	global_load_dwordx4 v[12:15], v[8:9], off offset:-16 nt
	global_load_dwordx4 v[16:19], v[8:9], off nt
	v_lshl_add_u64 v[10:11], v[10:11], 0, s[14:15]
	v_cmp_lt_u64_e32 vcc, s[24:25], v[10:11]
	v_lshl_add_u64 v[8:9], v[8:9], 0, s[10:11]
	s_or_b64 s[22:23], vcc, s[22:23]
	s_waitcnt vmcnt(1)
	v_bfe_u32 v1, v12, 16, 1
	v_bfe_u32 v20, v14, 16, 1
	s_waitcnt vmcnt(0)
	v_bfe_u32 v22, v16, 16, 1
	v_bfe_u32 v24, v18, 16, 1
	v_bfe_u32 v5, v13, 16, 1
	v_bfe_u32 v21, v15, 16, 1
	v_bfe_u32 v23, v17, 16, 1
	v_bfe_u32 v25, v19, 16, 1
	v_add3_u32 v1, v12, v1, s7
	v_add3_u32 v12, v14, v20, s7
	v_add3_u32 v14, v16, v22, s7
	v_add3_u32 v16, v18, v24, s7
	v_add3_u32 v5, v13, v5, s7
	v_add3_u32 v13, v15, v21, s7
	v_add3_u32 v15, v17, v23, s7
	v_add3_u32 v17, v19, v25, s7
	v_lshrrev_b32_e32 v1, 16, v1
	v_lshrrev_b32_e32 v18, 16, v12
	v_lshrrev_b32_e32 v14, 16, v14
	v_lshrrev_b32_e32 v16, 16, v16
	v_and_or_b32 v12, v5, s26, v1
	v_and_or_b32 v13, v13, s26, v18
	v_and_or_b32 v14, v15, s26, v14
	v_and_or_b32 v15, v17, s26, v16
	global_store_dwordx4 v[6:7], v[12:15], off
	v_lshl_add_u64 v[6:7], v[6:7], 0, s[20:21]
	s_andn2_b64 exec, exec, s[22:23]
	s_cbranch_execnz .LBB0_71

; __device__ __forceinline__ unsigned pk2(float lo, float hi) { return f2bf(lo) | (f2bf(hi) << 16); }
; __device__ __forceinline__ void cvt_stream(const float* src, bf16_t* dst, size_t n8, size_t gtid, size_t gthreads) {
;     for (size_t i = gtid; i < n8; i += gthreads) { const f32x4 a = ((const f32x4*)src)[2 * i], b = ((const f32x4*)src)[2 * i + 1];
;         ((u32x4*)dst)[i] = (u32x4){pk2(a.x, a.y), pk2(a.z, a.w), pk2(b.x, b.y), pk2(b.z, b.w)}; }
; }
; __device__ __forceinline__ void phase_prologue(const Frame& F, const Args& a) {
;     ...
;     cvt_stream(a.in[15], (bf16_t*)(ws + WS_SMALL + 4096), 128 * 128 / 8, gtid, gth);
;     cvt_stream(a.in[16], (bf16_t*)(ws + WS_SMALL + 4096 + 32768), 128 * 128 / 8, gtid, gth);
.LBB0_74:
	global_load_dwordx4 v[14:17], v[10:11], off offset:-16 nt
	global_load_dwordx4 v[18:21], v[10:11], off nt
	v_lshl_add_u64 v[12:13], v[12:13], 0, s[14:15]
	v_cmp_lt_u64_e32 vcc, s[22:23], v[12:13]
	v_lshl_add_u64 v[10:11], v[10:11], 0, s[18:19]
	s_or_b64 s[20:21], vcc, s[20:21]
	s_waitcnt vmcnt(1)
	v_bfe_u32 v1, v14, 16, 1
	v_bfe_u32 v22, v15, 16, 1
	v_bfe_u32 v23, v16, 16, 1
	v_bfe_u32 v24, v17, 16, 1
	s_waitcnt vmcnt(0)
	v_bfe_u32 v25, v18, 16, 1
	v_bfe_u32 v26, v19, 16, 1
	v_bfe_u32 v27, v20, 16, 1
	v_bfe_u32 v28, v21, 16, 1
	v_add3_u32 v1, v14, v1, s7
	v_add3_u32 v14, v15, v22, s7
	v_add3_u32 v15, v16, v23, s7
	v_add3_u32 v16, v17, v24, s7
	v_add3_u32 v17, v18, v25, s7
	v_add3_u32 v18, v19, v26, s7
	v_add3_u32 v19, v20, v27, s7
	v_add3_u32 v20, v21, v28, s7
	v_lshrrev_b32_e32 v1, 16, v1
	v_lshrrev_b32_e32 v15, 16, v15
	v_lshrrev_b32_e32 v17, 16, v17
	v_lshrrev_b32_e32 v19, 16, v19
	v_and_or_b32 v14, v14, s24, v1
	v_and_or_b32 v15, v16, s24, v15
	v_and_or_b32 v16, v18, s24, v17
	v_and_or_b32 v17, v20, s24, v19
	global_store_dwordx4 v[8:9], v[14:17], off
	v_lshl_add_u64 v[8:9], v[8:9], 0, s[16:17]
	s_andn2_b64 exec, exec, s[20:21]
	s_cbranch_execnz .LBB0_74
	s_or_b64 exec, exec, s[20:21]
	s_load_dwordx2 s[22:23], s[86:87], 0x80
	s_mov_b64 s[24:25], 0xf209000
	s_mov_b64 s[20:21], 0
	v_lshl_add_u64 v[6:7], v[6:7], 0, s[24:25]
	s_movk_i32 s7, 0x7fff
	s_waitcnt lgkmcnt(0)
	v_lshl_add_u64 v[4:5], s[22:23], 0, v[4:5]
	s_mov_b32 s24, 0xffff0000
	s_mov_b64 s[22:23], 0x7ff
.LBB0_76:
	global_load_dwordx4 v[8:11], v[4:5], off offset:-16 nt
	global_load_dwordx4 v[12:15], v[4:5], off nt
	v_lshl_add_u64 v[2:3], v[2:3], 0, s[14:15]
	v_cmp_lt_u64_e32 vcc, s[22:23], v[2:3]
	v_lshl_add_u64 v[4:5], v[4:5], 0, s[18:19]
	s_or_b64 s[20:21], vcc, s[20:21]
	s_waitcnt vmcnt(1)
	v_bfe_u32 v1, v8, 16, 1
	v_bfe_u32 v16, v9, 16, 1
	v_bfe_u32 v17, v10, 16, 1
	v_bfe_u32 v18, v11, 16, 1
	s_waitcnt vmcnt(0)
	v_bfe_u32 v19, v12, 16, 1
	v_bfe_u32 v20, v13, 16, 1
	v_bfe_u32 v21, v14, 16, 1
	v_bfe_u32 v22, v15, 16, 1
	v_add3_u32 v1, v8, v1, s7
	v_add3_u32 v8, v9, v16, s7
	v_add3_u32 v9, v10, v17, s7
	v_add3_u32 v10, v11, v18, s7
	v_add3_u32 v11, v12, v19, s7
	v_add3_u32 v12, v13, v20, s7
	v_add3_u32 v13, v14, v21, s7
	v_add3_u32 v14, v15, v22, s7
	v_lshrrev_b32_e32 v1, 16, v1
	v_lshrrev_b32_e32 v9, 16, v9
	v_lshrrev_b32_e32 v11, 16, v11
	v_lshrrev_b32_e32 v13, 16, v13
	v_and_or_b32 v8, v8, s24, v1
	v_and_or_b32 v9, v10, s24, v9
	v_and_or_b32 v10, v12, s24, v11
	v_and_or_b32 v11, v14, s24, v13
	global_store_dwordx4 v[6:7], v[8:11], off
	v_lshl_add_u64 v[6:7], v[6:7], 0, s[16:17]
	s_andn2_b64 exec, exec, s[20:21]
	s_cbranch_execnz .LBB0_76

; __device__ __forceinline__ float sigmoidf_(float x) { return __builtin_amdgcn_rcpf(1.f + __builtin_amdgcn_exp2f(-1.4426950408889634f * x)); }
; #define DMA(ti, slot) do { const int _b = __builtin_amdgcn_readfirstlane(list[ti]); int offK[2], offV[2]; dma_offsets(ldk, wid, lane, offK, offV); \
;         dma_tile(K_lds + (slot) * SHM, Kb, (size_t)_b * 64 * ldk, offK, wid); dma_tile(V_lds + (slot) * SHM, Vb, (size_t)_b * 64 * ldk, offV, wid); } while (0)
; template <int MODE> ...
;     ...
;     DMA(0, 0); if (n > 1) DMA(1, 1); if (n > 2) DMA(2, 2);
; __device__ __forceinline__ void attn_unit(const Frame& F, unsigned char* ws, int g, int qt) {
;     ...
;     const int hh = r32 >> 3, jt = r32 & 7, tl = 8 * wid + jt, t = t0 + tl, head = g * 4 + hh;
;     bf16x8 qr[8];
;     { const bf16_t* Qrow = Z + (size_t)t * ZW + ZC_Q + head * 128 + hi * 8;
; #pragma unroll
;       for (int d0 = 0; d0 < 8; ++d0) qr[d0] = *(const bf16x8*)(Qrow + d0 * 16); }
;     const float slope2 = __builtin_amdgcn_exp2f(-0.5f * (float)(head + 1)) * LOG2E;
;     const bf16_t* gz = Z + (size_t)t * ZW + ZC_G + head * 3;
;     const float g_cmp = sigmoidf_(bf2f(gz[0])), g_slc = sigmoidf_(bf2f(gz[1])), g_win = sigmoidf_(bf2f(gz[2]));
.LBB0_559:
	s_or_b64 exec, exec, s[2:3]
	v_readlane_b32 s2, v245, 51
	s_lshl_b32 s6, s67, 6
	s_and_b32 s31, s2, 3
	v_and_b32_e32 v158, 7, v157
	v_lshlrev_b32_e64 v10, 3, s30
	s_mov_b32 s2, s6
	s_waitcnt lgkmcnt(0)
	v_bfe_u32 v2, v157, 3, 2
	v_or_b32_e32 v172, v158, v10
	v_writelane_b32 v245, s2, 54
	v_ashrrev_i32_e32 v170, 5, v157
	v_add_u32_e32 v166, s6, v172
	v_writelane_b32 v245, s3, 55
	v_lshl_or_b32 v11, s31, 2, v2
	s_movk_i32 s2, 0x7a00
	v_mad_i64_i32 v[4:5], s[2:3], v166, s2, v[132:133]
	v_lshlrev_b32_e32 v2, 8, v11
	v_lshlrev_b32_e32 v8, 3, v170
	v_lshl_add_u64 v[6:7], v[4:5], 0, v[2:3]
	v_ashrrev_i32_e32 v9, 31, v8
	v_lshl_add_u64 v[6:7], v[8:9], 1, v[6:7]
	s_mov_b64 s[2:3], 0x1000
	v_lshl_add_u64 v[8:9], v[6:7], 0, s[2:3]
	s_movk_i32 s2, 0x1000
	v_add_co_u32_e32 v6, vcc, s2, v6
	s_waitcnt lgkmcnt(0)
	s_barrier
	v_addc_co_u32_e32 v7, vcc, 0, v7, vcc
	global_load_dwordx4 v[100:103], v[8:9], off offset:32 nt
	global_load_dwordx4 v[104:107], v[8:9], off offset:64 nt
	global_load_dwordx4 v[108:111], v[8:9], off offset:96 nt
	global_load_dwordx4 v[112:115], v[8:9], off offset:128 nt
	global_load_dwordx4 v[116:119], v[8:9], off offset:160 nt
	global_load_dwordx4 v[120:123], v[8:9], off offset:192 nt
	global_load_dwordx4 v[124:127], v[6:7], off nt
	global_load_dwordx4 v[128:131], v[8:9], off offset:224 nt
	v_mul_u32_u24_e32 v2, 3, v11
	v_lshlrev_b32_e32 v2, 1, v2
	v_lshl_add_u64 v[4:5], v[4:5], 0, v[2:3]
	s_mov_b64 s[2:3], 0x3800
	v_lshl_add_u64 v[6:7], v[4:5], 0, s[2:3]
	s_movk_i32 s2, 0x3000
	v_add_co_u32_e32 v4, vcc, s2, v4
	v_add_u32_e32 v2, 1, v11
	s_nop 0
	v_addc_co_u32_e32 v5, vcc, 0, v5, vcc
	global_load_dword v171, v[4:5], off offset:2048
	global_load_ushort v164, v[6:7], off offset:4
	v_cvt_f32_ubyte0_e32 v2, v2
	v_mul_f32_e32 v2, -0.5, v2
	ds_read_b32 v4, v1
	ds_read_b32 v5, v160
	v_exp_f32_e32 v2, v2
	v_readfirstlane_b32 s2, v10
	v_lshlrev_b32_e64 v6, 8, s30
	v_lshlrev_b32_e32 v154, 4, v157
	v_writelane_b32 v245, s2, 56
	v_mul_f32_e32 v134, 0x3fb8aa3b, v2
	v_add_u32_e32 v146, 0, v6
	v_writelane_b32 v245, s3, 57
	s_waitcnt lgkmcnt(0)
	v_readfirstlane_b32 s2, v5
	v_lshlrev_b32_e32 v2, 3, v157
	v_and_b32_e32 v5, 0xc0, v154
	v_lshlrev_b32_e32 v6, 1, v157
	v_writelane_b32 v245, s2, 58
	v_and_or_b32 v5, v2, 24, v5
	v_and_b32_e32 v6, 32, v6
	v_and_b32_e32 v2, 0x100, v2
	s_lshl_b32 s2, s31, 17
	v_readlane_b32 s3, v245, 18
	v_or3_b32 v2, v5, v6, v2
	v_readfirstlane_b32 s18, v4
	s_add_u32 s14, s3, s2
	v_readlane_b32 s2, v245, 19
	v_add_u32_e32 v165, 0, v2
	v_cmp_gt_i32_e32 vcc, 1, v4
	v_ashrrev_i32_e32 v159, 4, v157
	v_and_b32_e32 v173, 15, v157
	v_bfe_u32 v2, v157, 2, 2
	v_lshrrev_b32_e32 v4, 1, v157
	v_and_b32_e32 v153, 3, v157
	v_lshrrev_b32_e32 v5, 7, v154
	v_and_b32_e32 v163, 31, v157
	s_addc_u32 s15, s2, 0
	v_readfirstlane_b32 s97, v146
	v_add_u32_e32 v168, 0x18080, v146
	v_and_or_b32 v155, v4, 8, v2
	v_bitop3_b32 v174, v159, v173, 7 bitop3:0x6c
	v_and_or_b32 v156, v5, 12, v153
	s_cbranch_vccnz .LBB0_574
	s_add_u32 s19, s14, 0x80000
	s_addc_u32 s20, s15, 0
	s_add_i32 s6, 0, 0x21020
	v_mov_b32_e32 v2, s6
	ds_read_b32 v2, v2
	s_lshl_b32 s2, s30, 10
	s_lshl_b32 s7, s30, 11
	v_lshl_add_u32 v4, v159, 7, s2
	v_lshl_or_b32 v136, v174, 3, v4
	s_waitcnt lgkmcnt(0)
	v_readfirstlane_b32 s2, v2
	v_add_u32_e32 v2, s7, v154
	v_ashrrev_i32_e32 v2, 8, v2
	v_and_b32_e32 v4, 0x1fffff0, v2
	v_lshrrev_b32_e32 v2, 1, v2
	s_lshl_b32 s3, s30, 1
	v_and_b32_e32 v2, 4, v2
	v_or3_b32 v2, v4, v2, v155
	v_lshlrev_b32_e32 v4, 3, v156
	s_or_b32 s3, s3, 1
	v_lshl_or_b32 v138, v2, 7, v4
	v_lshl_add_u32 v2, s3, 2, v159
	v_bitop3_b32 v4, v2, v173, 7 bitop3:0x6c
	v_lshlrev_b32_e32 v2, 7, v2
	v_lshl_or_b32 v140, v4, 3, v2
	v_lshl_add_u32 v2, s3, 10, v154
	s_ashr_i32 s3, s2, 31
	v_ashrrev_i32_e32 v4, 8, v2
	s_lshl_b64 s[2:3], s[2:3], 14
	v_and_b32_e32 v5, 0x1fffff0, v4
	v_lshrrev_b32_e32 v4, 1, v4
	v_lshrrev_b32_e32 v2, 7, v2
	s_add_u32 s10, s14, s2
	v_and_b32_e32 v4, 4, v4
	v_and_or_b32 v2, v2, 12, v153
	s_addc_u32 s11, s15, s3
	s_add_i32 s21, s7, 0
	v_or3_b32 v4, v5, v4, v155
	v_lshlrev_b32_e32 v2, 3, v2
	s_add_i32 s24, s21, 0xc000
	v_ashrrev_i32_e32 v137, 31, v136
	s_add_i32 s23, s21, 0xc400
	v_lshl_or_b32 v142, v4, 7, v2
	v_lshl_add_u64 v[4:5], v[136:137], 1, s[10:11]
	s_mov_b32 m0, s24
	v_ashrrev_i32_e32 v141, 31, v140
	s_add_u32 s2, s19, s2
	global_load_lds_dwordx4 v[4:5], off
	v_lshl_add_u64 v[4:5], v[140:141], 1, s[10:11]
	s_mov_b32 m0, s23
	s_addc_u32 s3, s20, s3
	v_ashrrev_i32_e32 v139, 31, v138
	global_load_lds_dwordx4 v[4:5], off
	v_lshl_add_u64 v[4:5], v[138:139], 1, s[2:3]
	s_mov_b32 m0, s21
	v_ashrrev_i32_e32 v143, 31, v142
	s_add_i32 s25, s21, 0x400
	global_load_lds_dwordx4 v[4:5], off
	v_lshl_add_u64 v[4:5], v[142:143], 1, s[2:3]
	s_mov_b32 m0, s25
	s_cmp_lg_u32 s18, 1
	global_load_lds_dwordx4 v[4:5], off
	s_cselect_b64 s[12:13], -1, 0
	s_cmp_eq_u32 s18, 1
	s_cbranch_scc1 .LBB0_562
	v_readlane_b32 s2, v245, 31
	s_nop 1
	v_mov_b32_e32 v2, s2
	ds_read_b32 v2, v2
	s_waitcnt lgkmcnt(0)
	v_readfirstlane_b32 s2, v2
	s_ashr_i32 s3, s2, 31
	s_lshl_b64 s[2:3], s[2:3], 14
	s_add_u32 s10, s14, s2
	s_addc_u32 s11, s15, s3
	s_add_i32 m0, s21, 0x10000
	v_lshl_add_u64 v[4:5], v[136:137], 1, s[10:11]
	global_load_lds_dwordx4 v[4:5], off
	s_add_i32 m0, s21, 0x10400
	s_add_u32 s2, s19, s2
	v_lshl_add_u64 v[4:5], v[140:141], 1, s[10:11]
	s_addc_u32 s3, s20, s3
	global_load_lds_dwordx4 v[4:5], off
	v_lshl_add_u64 v[4:5], v[138:139], 1, s[2:3]
	s_add_i32 m0, s21, 0x4000
	s_nop 0
	global_load_lds_dwordx4 v[4:5], off
	v_lshl_add_u64 v[4:5], v[142:143], 1, s[2:3]
	s_add_i32 m0, s21, 0x4400
	s_nop 0
	global_load_lds_dwordx4 v[4:5], off
